# out-projection epilogue: the 16 residual tiles of each lane loaded up front (single wait), stores no longer acknowledged between tiles
# baseline (speedup 1.0000x reference)
; __device__ __forceinline__ unsigned cvt_pk_bf16(float lo, float hi) { unsigned r; asm volatile("v_cvt_pk_bf16_f32 %0, %1, %2" : "=v"(r) : "v"(lo), "v"(hi)); return r; }
;     __device__ __forceinline__ void operator()(const f32x4 (&acc)[2][2][4][2], const Unit& u, int wr, int wc, int fr, int fq) const {
;         const int row0 = u.pm * BM + wr * 64 + fr, col0 = u.pn * BM + wc * 32 + 8 * fq;
;         const float* gb = gate + (size_t)((u.pm * BM) >> 13) * 6144 + col0;
;         f32x4 gv[2][2];
; #pragma unroll
;         for (int bj = 0; bj < 2; ++bj)
; #pragma unroll
;             for (int n = 0; n < 2; ++n) gv[bj][n] = *(const f32x4*)(gb + bj * HALF + n * 4);
; #pragma unroll
;         for (int ai = 0; ai < 2; ++ai)
; #pragma unroll
;             for (int m = 0; m < 4; ++m) { bf16_t* rowp = X + (size_t)(row0 + ai * HALF + m * 16) * 1024 + col0;
; #pragma unroll
;                 for (int bj = 0; bj < 2; ++bj) { const u32x4 xr = *(const u32x4*)(rowp + bj * HALF);
;                     f32x4 x0, x1; x0[0] = __uint_as_float(xr.x << 16); x0[1] = __uint_as_float(xr.x & 0xffff0000u); x0[2] = __uint_as_float(xr.y << 16); x0[3] = __uint_as_float(xr.y & 0xffff0000u);
;                     x1[0] = __uint_as_float(xr.z << 16); x1[1] = __uint_as_float(xr.z & 0xffff0000u); x1[2] = __uint_as_float(xr.w << 16); x1[3] = __uint_as_float(xr.w & 0xffff0000u);
;                     x0 = x0 + gv[bj][0] * acc[ai][bj][m][0]; x1 = x1 + gv[bj][1] * acc[ai][bj][m][1];
;                     u32x4 w; w.x = cvt_pk_bf16(x0[0], x0[1]); w.y = cvt_pk_bf16(x0[2], x0[3]); w.z = cvt_pk_bf16(x1[0], x1[1]); w.w = cvt_pk_bf16(x1[2], x1[3]);
;                     *(u32x4*)(rowp + bj * HALF) = w; } }
.LBB0_3171:
	v_lshl_add_u32 v160, s18, 8, v1
	v_lshl_or_b32 v116, s62, 8, v165
	v_ashrrev_i32_e32 v161, 31, v160
	v_ashrrev_i32_e32 v117, 31, v116
	v_lshlrev_b64 v[118:119], 11, v[160:161]
	v_lshl_add_u64 v[118:119], s[6:7], 0, v[118:119]
	v_lshlrev_b64 v[162:163], 1, v[116:117]
	s_ashr_i32 s11, s18, 5
	v_lshl_add_u64 v[158:159], v[118:119], 0, v[162:163]
	s_mul_hi_i32 s13, s11, 0x6000
	s_mulk_i32 s11, 0x6000
	v_mov_b32_e32 v176, v158
	v_mov_b32_e32 v177, v159
	s_mov_b64 s[72:73], 0x8000
	s_mov_b64 s[74:75], 0x28000
	global_load_dwordx4 v[180:183], v[176:177], off
	global_load_dwordx4 v[184:187], v[176:177], off offset:256
	v_lshl_add_u64 v[176:177], v[176:177], 0, s[72:73]
	global_load_dwordx4 v[188:191], v[176:177], off
	global_load_dwordx4 v[192:195], v[176:177], off offset:256
	v_lshl_add_u64 v[176:177], v[176:177], 0, s[72:73]
	global_load_dwordx4 v[196:199], v[176:177], off
	global_load_dwordx4 v[200:203], v[176:177], off offset:256
	v_lshl_add_u64 v[176:177], v[176:177], 0, s[72:73]
	global_load_dwordx4 v[204:207], v[176:177], off
	global_load_dwordx4 v[208:211], v[176:177], off offset:256
	v_lshl_add_u64 v[176:177], v[176:177], 0, s[74:75]
	global_load_dwordx4 v[212:215], v[176:177], off
	global_load_dwordx4 v[218:221], v[176:177], off offset:256
	v_lshl_add_u64 v[176:177], v[176:177], 0, s[72:73]
	global_load_dwordx4 v[224:227], v[176:177], off
	global_load_dwordx4 v[238:241], v[176:177], off offset:256
	v_lshl_add_u64 v[176:177], v[176:177], 0, s[72:73]
	global_load_dwordx4 v[242:245], v[176:177], off
	global_load_dwordx4 v[246:249], v[176:177], off offset:256
	v_lshl_add_u64 v[176:177], v[176:177], 0, s[72:73]
	global_load_dwordx4 v[250:253], v[176:177], off
	global_load_dwordx4 v[176:179], v[176:177], off offset:256
	s_add_u32 s20, s44, s11
	s_addc_u32 s21, s45, s13
	v_lshl_add_u64 v[120:121], v[116:117], 2, s[20:21]
	global_load_dwordx4 v[136:139], v[120:121], off
	global_load_dwordx4 v[132:135], v[120:121], off offset:16
	global_load_dwordx4 v[116:119], v[120:121], off offset:528
	s_nop 0
	global_load_dwordx4 v[120:123], v[120:121], off offset:512
	s_mov_b32 s11, 0x40000
	s_mov_b64 s[20:21], 0x40000
	s_waitcnt vmcnt(0)
	v_mov_b32_e32 v168, v180
	v_mov_b32_e32 v169, v181
	v_mov_b32_e32 v170, v182
	v_mov_b32_e32 v171, v183
	v_lshlrev_b32_e32 v172, 16, v168
	v_and_b32_e32 v173, 0xffff0000, v168
	v_lshlrev_b32_e32 v168, 16, v169
	v_and_b32_e32 v169, 0xffff0000, v169
	v_lshlrev_b32_e32 v174, 16, v170
	v_and_b32_e32 v175, 0xffff0000, v170
	v_lshlrev_b32_e32 v170, 16, v171
	v_and_b32_e32 v171, 0xffff0000, v171
	v_pk_fma_f32 v[146:147], v[146:147], v[138:139], v[168:169]
	v_pk_fma_f32 v[144:145], v[144:145], v[136:137], v[172:173]
	v_pk_fma_f32 v[168:169], v[142:143], v[134:135], v[170:171]
	v_pk_fma_f32 v[142:143], v[140:141], v[132:133], v[174:175]
	v_cvt_pk_bf16_f32 v140, v144, v145
	v_cvt_pk_bf16_f32 v141, v146, v147
	s_nop 0
	v_cvt_pk_bf16_f32 v142, v142, v143
	v_cvt_pk_bf16_f32 v143, v168, v169
	s_nop 0
	v_or_b32_e32 v168, 16, v160
	v_ashrrev_i32_e32 v169, 31, v168
	v_lshlrev_b64 v[168:169], 11, v[168:169]
	v_lshl_add_u64 v[168:169], s[6:7], 0, v[168:169]
	global_store_dwordx4 v[158:159], v[140:143], off
	v_lshl_add_u64 v[168:169], v[168:169], 0, v[162:163]
	v_mov_b32_e32 v144, v184
	v_mov_b32_e32 v145, v185
	v_mov_b32_e32 v146, v186
	v_mov_b32_e32 v147, v187
	v_lshlrev_b32_e32 v140, 16, v144
	v_and_b32_e32 v141, 0xffff0000, v144
	v_lshlrev_b32_e32 v142, 16, v145
	v_and_b32_e32 v143, 0xffff0000, v145
	v_lshlrev_b32_e32 v144, 16, v146
	v_and_b32_e32 v145, 0xffff0000, v146
	v_lshlrev_b32_e32 v146, 16, v147
	v_and_b32_e32 v147, 0xffff0000, v147
	v_pk_fma_f32 v[126:127], v[126:127], v[122:123], v[142:143]
	v_pk_fma_f32 v[124:125], v[124:125], v[120:121], v[140:141]
	v_pk_fma_f32 v[140:141], v[114:115], v[118:119], v[146:147]
	v_pk_fma_f32 v[114:115], v[112:113], v[116:117], v[144:145]
	v_cvt_pk_bf16_f32 v112, v124, v125
	v_cvt_pk_bf16_f32 v113, v126, v127
	s_nop 0
	v_cvt_pk_bf16_f32 v114, v114, v115
	v_cvt_pk_bf16_f32 v115, v140, v141
	s_nop 0
	s_nop 0
	global_store_dwordx4 v[158:159], v[112:115], off offset:256
	v_mov_b32_e32 v124, v188
	v_mov_b32_e32 v125, v189
	v_mov_b32_e32 v126, v190
	v_mov_b32_e32 v127, v191
	s_nop 0
	v_lshlrev_b32_e32 v112, 16, v124
	v_and_b32_e32 v113, 0xffff0000, v124
	v_lshlrev_b32_e32 v114, 16, v125
	v_and_b32_e32 v115, 0xffff0000, v125
	v_lshlrev_b32_e32 v124, 16, v126
	v_and_b32_e32 v125, 0xffff0000, v126
	v_lshlrev_b32_e32 v126, 16, v127
	v_and_b32_e32 v127, 0xffff0000, v127
	v_pk_fma_f32 v[114:115], v[130:131], v[138:139], v[114:115]
	v_pk_fma_f32 v[112:113], v[128:129], v[136:137], v[112:113]
	v_pk_fma_f32 v[126:127], v[110:111], v[134:135], v[126:127]
	v_pk_fma_f32 v[110:111], v[108:109], v[132:133], v[124:125]
	v_cvt_pk_bf16_f32 v108, v112, v113
	v_cvt_pk_bf16_f32 v109, v114, v115
	v_or_b32_e32 v124, 32, v160
	v_cvt_pk_bf16_f32 v110, v110, v111
	v_cvt_pk_bf16_f32 v111, v126, v127
	s_nop 0
	v_ashrrev_i32_e32 v125, 31, v124
	v_lshlrev_b64 v[124:125], 11, v[124:125]
	v_lshl_add_u64 v[124:125], s[6:7], 0, v[124:125]
	global_store_dwordx4 v[168:169], v[108:111], off
	v_lshl_add_u64 v[124:125], v[124:125], 0, v[162:163]
	v_mov_b32_e32 v112, v192
	v_mov_b32_e32 v113, v193
	v_mov_b32_e32 v114, v194
	v_mov_b32_e32 v115, v195
	v_lshlrev_b32_e32 v108, 16, v112
	v_and_b32_e32 v109, 0xffff0000, v112
	v_lshlrev_b32_e32 v110, 16, v113
	v_and_b32_e32 v111, 0xffff0000, v113
	v_lshlrev_b32_e32 v112, 16, v114
	v_and_b32_e32 v113, 0xffff0000, v114
	v_lshlrev_b32_e32 v114, 16, v115
	v_and_b32_e32 v115, 0xffff0000, v115
	v_pk_fma_f32 v[102:103], v[102:103], v[122:123], v[110:111]
	v_pk_fma_f32 v[100:101], v[100:101], v[120:121], v[108:109]
; __device__ __forceinline__ unsigned cvt_pk_bf16(float lo, float hi) { unsigned r; asm volatile("v_cvt_pk_bf16_f32 %0, %1, %2" : "=v"(r) : "v"(lo), "v"(hi)); return r; }
;     __device__ __forceinline__ void operator()(const f32x4 (&acc)[2][2][4][2], const Unit& u, int wr, int wc, int fr, int fq) const {
;     ...
;         for (int ai = 0; ai < 2; ++ai)
; #pragma unroll
;             for (int m = 0; m < 4; ++m) { bf16_t* rowp = X + (size_t)(row0 + ai * HALF + m * 16) * 1024 + col0;
; #pragma unroll
;                 for (int bj = 0; bj < 2; ++bj) { const u32x4 xr = *(const u32x4*)(rowp + bj * HALF);
;                     f32x4 x0, x1; x0[0] = __uint_as_float(xr.x << 16); x0[1] = __uint_as_float(xr.x & 0xffff0000u); x0[2] = __uint_as_float(xr.y << 16); x0[3] = __uint_as_float(xr.y & 0xffff0000u);
;                     x1[0] = __uint_as_float(xr.z << 16); x1[1] = __uint_as_float(xr.z & 0xffff0000u); x1[2] = __uint_as_float(xr.w << 16); x1[3] = __uint_as_float(xr.w & 0xffff0000u);
;                     x0 = x0 + gv[bj][0] * acc[ai][bj][m][0]; x1 = x1 + gv[bj][1] * acc[ai][bj][m][1];
;                     u32x4 w; w.x = cvt_pk_bf16(x0[0], x0[1]); w.y = cvt_pk_bf16(x0[2], x0[3]); w.z = cvt_pk_bf16(x1[0], x1[1]); w.w = cvt_pk_bf16(x1[2], x1[3]);
;                     *(u32x4*)(rowp + bj * HALF) = w; } }
	v_pk_fma_f32 v[108:109], v[98:99], v[118:119], v[114:115]
	v_pk_fma_f32 v[98:99], v[96:97], v[116:117], v[112:113]
	v_cvt_pk_bf16_f32 v96, v100, v101
	v_cvt_pk_bf16_f32 v97, v102, v103
	s_nop 0
	v_cvt_pk_bf16_f32 v98, v98, v99
	v_cvt_pk_bf16_f32 v99, v108, v109
	s_nop 0
	s_nop 0
	global_store_dwordx4 v[168:169], v[96:99], off offset:256
	v_mov_b32_e32 v100, v196
	v_mov_b32_e32 v101, v197
	v_mov_b32_e32 v102, v198
	v_mov_b32_e32 v103, v199
	s_nop 0
	v_lshlrev_b32_e32 v96, 16, v100
	v_and_b32_e32 v97, 0xffff0000, v100
	v_lshlrev_b32_e32 v98, 16, v101
	v_and_b32_e32 v99, 0xffff0000, v101
	v_lshlrev_b32_e32 v100, 16, v102
	v_and_b32_e32 v101, 0xffff0000, v102
	v_lshlrev_b32_e32 v102, 16, v103
	v_and_b32_e32 v103, 0xffff0000, v103
	v_pk_fma_f32 v[98:99], v[106:107], v[138:139], v[98:99]
	v_pk_fma_f32 v[96:97], v[104:105], v[136:137], v[96:97]
	v_pk_fma_f32 v[102:103], v[94:95], v[134:135], v[102:103]
	v_pk_fma_f32 v[94:95], v[92:93], v[132:133], v[100:101]
	v_cvt_pk_bf16_f32 v92, v96, v97
	v_cvt_pk_bf16_f32 v93, v98, v99
	v_or_b32_e32 v100, 48, v160
	v_cvt_pk_bf16_f32 v94, v94, v95
	v_cvt_pk_bf16_f32 v95, v102, v103
	s_nop 0
	v_ashrrev_i32_e32 v101, 31, v100
	v_lshlrev_b64 v[100:101], 11, v[100:101]
	v_lshl_add_u64 v[100:101], s[6:7], 0, v[100:101]
	global_store_dwordx4 v[124:125], v[92:95], off
	v_lshl_add_u64 v[100:101], v[100:101], 0, v[162:163]
	v_mov_b32_e32 v96, v200
	v_mov_b32_e32 v97, v201
	v_mov_b32_e32 v98, v202
	v_mov_b32_e32 v99, v203
	v_lshlrev_b32_e32 v92, 16, v96
	v_and_b32_e32 v93, 0xffff0000, v96
	v_lshlrev_b32_e32 v94, 16, v97
	v_and_b32_e32 v95, 0xffff0000, v97
	v_lshlrev_b32_e32 v96, 16, v98
	v_and_b32_e32 v97, 0xffff0000, v98
	v_lshlrev_b32_e32 v98, 16, v99
	v_and_b32_e32 v99, 0xffff0000, v99
	v_pk_fma_f32 v[86:87], v[86:87], v[122:123], v[94:95]
	v_pk_fma_f32 v[84:85], v[84:85], v[120:121], v[92:93]
	v_pk_fma_f32 v[92:93], v[82:83], v[118:119], v[98:99]
	v_pk_fma_f32 v[82:83], v[80:81], v[116:117], v[96:97]
	v_cvt_pk_bf16_f32 v80, v84, v85
	v_cvt_pk_bf16_f32 v81, v86, v87
	s_nop 0
	v_cvt_pk_bf16_f32 v82, v82, v83
	v_cvt_pk_bf16_f32 v83, v92, v93
	s_nop 0
	s_nop 0
	global_store_dwordx4 v[124:125], v[80:83], off offset:256
	v_mov_b32_e32 v84, v204
	v_mov_b32_e32 v85, v205
	v_mov_b32_e32 v86, v206
	v_mov_b32_e32 v87, v207
	s_nop 0
	v_lshlrev_b32_e32 v80, 16, v84
	v_and_b32_e32 v81, 0xffff0000, v84
	v_lshlrev_b32_e32 v82, 16, v85
	v_and_b32_e32 v83, 0xffff0000, v85
	v_lshlrev_b32_e32 v84, 16, v86
	v_and_b32_e32 v85, 0xffff0000, v86
	v_lshlrev_b32_e32 v86, 16, v87
	v_and_b32_e32 v87, 0xffff0000, v87
	v_pk_fma_f32 v[82:83], v[90:91], v[138:139], v[82:83]
	v_pk_fma_f32 v[80:81], v[88:89], v[136:137], v[80:81]
	v_pk_fma_f32 v[86:87], v[78:79], v[134:135], v[86:87]
	v_pk_fma_f32 v[78:79], v[76:77], v[132:133], v[84:85]
	v_cvt_pk_bf16_f32 v76, v80, v81
	v_cvt_pk_bf16_f32 v77, v82, v83
	v_add_co_u32_e32 v84, vcc, s11, v158
	v_cvt_pk_bf16_f32 v78, v78, v79
	v_cvt_pk_bf16_f32 v79, v86, v87
	s_nop 0
	s_nop 0
	v_addc_co_u32_e32 v85, vcc, 0, v159, vcc
	global_store_dwordx4 v[100:101], v[76:79], off
	s_mov_b32 s11, 0x48000
	v_mov_b32_e32 v80, v208
	v_mov_b32_e32 v81, v209
	v_mov_b32_e32 v82, v210
	v_mov_b32_e32 v83, v211
	v_lshlrev_b32_e32 v76, 16, v80
	v_and_b32_e32 v77, 0xffff0000, v80
	v_lshlrev_b32_e32 v78, 16, v81
	v_and_b32_e32 v79, 0xffff0000, v81
	v_lshlrev_b32_e32 v80, 16, v82
	v_and_b32_e32 v81, 0xffff0000, v82
	v_lshlrev_b32_e32 v82, 16, v83
	v_and_b32_e32 v83, 0xffff0000, v83
	v_pk_fma_f32 v[74:75], v[74:75], v[122:123], v[78:79]
	v_pk_fma_f32 v[72:73], v[72:73], v[120:121], v[76:77]
	v_pk_fma_f32 v[76:77], v[70:71], v[118:119], v[82:83]
	v_pk_fma_f32 v[70:71], v[68:69], v[116:117], v[80:81]
	v_cvt_pk_bf16_f32 v68, v72, v73
	v_cvt_pk_bf16_f32 v69, v74, v75
	s_nop 0
	v_cvt_pk_bf16_f32 v70, v70, v71
	v_cvt_pk_bf16_f32 v71, v76, v77
	s_nop 0
	v_lshl_add_u64 v[76:77], v[158:159], 0, s[20:21]
	global_store_dwordx4 v[100:101], v[68:71], off offset:256
	s_mov_b64 s[20:21], 0x48000
	v_mov_b32_e32 v72, v212
	v_mov_b32_e32 v73, v213
	v_mov_b32_e32 v74, v214
	v_mov_b32_e32 v75, v215
	v_lshlrev_b32_e32 v68, 16, v72
	v_and_b32_e32 v69, 0xffff0000, v72
	v_lshlrev_b32_e32 v70, 16, v73
	v_and_b32_e32 v71, 0xffff0000, v73
	v_lshlrev_b32_e32 v72, 16, v74
	v_and_b32_e32 v73, 0xffff0000, v74
	v_lshlrev_b32_e32 v74, 16, v75
	v_and_b32_e32 v75, 0xffff0000, v75
	v_pk_fma_f32 v[66:67], v[66:67], v[138:139], v[70:71]
	v_pk_fma_f32 v[64:65], v[64:65], v[136:137], v[68:69]
	v_pk_fma_f32 v[68:69], v[62:63], v[134:135], v[74:75]
	v_pk_fma_f32 v[62:63], v[60:61], v[132:133], v[72:73]
	v_cvt_pk_bf16_f32 v60, v64, v65
	v_cvt_pk_bf16_f32 v61, v66, v67
	s_nop 0
	v_cvt_pk_bf16_f32 v62, v62, v63
	v_cvt_pk_bf16_f32 v63, v68, v69
	s_nop 0
	v_add_co_u32_e32 v68, vcc, s11, v158
	global_store_dwordx4 v[84:85], v[60:63], off
	s_nop 0
	v_addc_co_u32_e32 v69, vcc, 0, v159, vcc
	s_mov_b32 s11, 0x50000
	v_mov_b32_e32 v64, v218
	v_mov_b32_e32 v65, v219
	v_mov_b32_e32 v66, v220
	v_mov_b32_e32 v67, v221
	v_lshlrev_b32_e32 v60, 16, v64
	v_and_b32_e32 v61, 0xffff0000, v64
	v_lshlrev_b32_e32 v62, 16, v65
	v_and_b32_e32 v63, 0xffff0000, v65
	v_lshlrev_b32_e32 v64, 16, v66
	v_and_b32_e32 v65, 0xffff0000, v66
	v_lshlrev_b32_e32 v66, 16, v67
	v_and_b32_e32 v67, 0xffff0000, v67
	v_pk_fma_f32 v[58:59], v[58:59], v[122:123], v[62:63]
	v_pk_fma_f32 v[56:57], v[56:57], v[120:121], v[60:61]
	v_pk_fma_f32 v[60:61], v[50:51], v[118:119], v[66:67]
	v_pk_fma_f32 v[50:51], v[48:49], v[116:117], v[64:65]
	v_cvt_pk_bf16_f32 v48, v56, v57
; __device__ __forceinline__ unsigned cvt_pk_bf16(float lo, float hi) { unsigned r; asm volatile("v_cvt_pk_bf16_f32 %0, %1, %2" : "=v"(r) : "v"(lo), "v"(hi)); return r; }
;     __device__ __forceinline__ void operator()(const f32x4 (&acc)[2][2][4][2], const Unit& u, int wr, int wc, int fr, int fq) const {
;     ...
;         for (int ai = 0; ai < 2; ++ai)
; #pragma unroll
;             for (int m = 0; m < 4; ++m) { bf16_t* rowp = X + (size_t)(row0 + ai * HALF + m * 16) * 1024 + col0;
; #pragma unroll
;                 for (int bj = 0; bj < 2; ++bj) { const u32x4 xr = *(const u32x4*)(rowp + bj * HALF);
;                     f32x4 x0, x1; x0[0] = __uint_as_float(xr.x << 16); x0[1] = __uint_as_float(xr.x & 0xffff0000u); x0[2] = __uint_as_float(xr.y << 16); x0[3] = __uint_as_float(xr.y & 0xffff0000u);
;                     x1[0] = __uint_as_float(xr.z << 16); x1[1] = __uint_as_float(xr.z & 0xffff0000u); x1[2] = __uint_as_float(xr.w << 16); x1[3] = __uint_as_float(xr.w & 0xffff0000u);
;                     x0 = x0 + gv[bj][0] * acc[ai][bj][m][0]; x1 = x1 + gv[bj][1] * acc[ai][bj][m][1];
;                     u32x4 w; w.x = cvt_pk_bf16(x0[0], x0[1]); w.y = cvt_pk_bf16(x0[2], x0[3]); w.z = cvt_pk_bf16(x1[0], x1[1]); w.w = cvt_pk_bf16(x1[2], x1[3]);
;                     *(u32x4*)(rowp + bj * HALF) = w; } }
	v_cvt_pk_bf16_f32 v49, v58, v59
	s_nop 0
	v_cvt_pk_bf16_f32 v50, v50, v51
	v_cvt_pk_bf16_f32 v51, v60, v61
	s_nop 0
	v_lshl_add_u64 v[60:61], v[158:159], 0, s[20:21]
	global_store_dwordx4 v[76:77], v[48:51], off offset:256
	s_mov_b64 s[20:21], 0x50000
	v_mov_b32_e32 v56, v224
	v_mov_b32_e32 v57, v225
	v_mov_b32_e32 v58, v226
	v_mov_b32_e32 v59, v227
	v_lshlrev_b32_e32 v48, 16, v56
	v_and_b32_e32 v49, 0xffff0000, v56
	v_lshlrev_b32_e32 v50, 16, v57
	v_and_b32_e32 v51, 0xffff0000, v57
	v_lshlrev_b32_e32 v56, 16, v58
	v_and_b32_e32 v57, 0xffff0000, v58
	v_lshlrev_b32_e32 v58, 16, v59
	v_and_b32_e32 v59, 0xffff0000, v59
	v_pk_fma_f32 v[50:51], v[54:55], v[138:139], v[50:51]
	v_pk_fma_f32 v[48:49], v[52:53], v[136:137], v[48:49]
	v_pk_fma_f32 v[52:53], v[46:47], v[134:135], v[58:59]
	v_pk_fma_f32 v[46:47], v[44:45], v[132:133], v[56:57]
	v_cvt_pk_bf16_f32 v44, v48, v49
	v_cvt_pk_bf16_f32 v45, v50, v51
	s_nop 0
	v_cvt_pk_bf16_f32 v46, v46, v47
	v_cvt_pk_bf16_f32 v47, v52, v53
	s_nop 0
	v_add_co_u32_e32 v52, vcc, s11, v158
	global_store_dwordx4 v[68:69], v[44:47], off
	s_nop 0
	v_addc_co_u32_e32 v53, vcc, 0, v159, vcc
	s_mov_b32 s11, 0x58000
	v_mov_b32_e32 v48, v238
	v_mov_b32_e32 v49, v239
	v_mov_b32_e32 v50, v240
	v_mov_b32_e32 v51, v241
	v_lshlrev_b32_e32 v44, 16, v48
	v_and_b32_e32 v45, 0xffff0000, v48
	v_lshlrev_b32_e32 v46, 16, v49
	v_and_b32_e32 v47, 0xffff0000, v49
	v_lshlrev_b32_e32 v48, 16, v50
	v_and_b32_e32 v49, 0xffff0000, v50
	v_lshlrev_b32_e32 v50, 16, v51
	v_and_b32_e32 v51, 0xffff0000, v51
	v_pk_fma_f32 v[42:43], v[42:43], v[122:123], v[46:47]
	v_pk_fma_f32 v[40:41], v[40:41], v[120:121], v[44:45]
	v_pk_fma_f32 v[44:45], v[34:35], v[118:119], v[50:51]
	v_pk_fma_f32 v[34:35], v[32:33], v[116:117], v[48:49]
	v_cvt_pk_bf16_f32 v32, v40, v41
	v_cvt_pk_bf16_f32 v33, v42, v43
	s_nop 0
	v_cvt_pk_bf16_f32 v34, v34, v35
	v_cvt_pk_bf16_f32 v35, v44, v45
	s_nop 0
	v_lshl_add_u64 v[44:45], v[158:159], 0, s[20:21]
	global_store_dwordx4 v[60:61], v[32:35], off offset:256
	s_mov_b64 s[20:21], 0x58000
	v_mov_b32_e32 v40, v242
	v_mov_b32_e32 v41, v243
	v_mov_b32_e32 v42, v244
	v_mov_b32_e32 v43, v245
	v_lshlrev_b32_e32 v32, 16, v40
	v_and_b32_e32 v33, 0xffff0000, v40
	v_lshlrev_b32_e32 v34, 16, v41
	v_and_b32_e32 v35, 0xffff0000, v41
	v_lshlrev_b32_e32 v40, 16, v42
	v_and_b32_e32 v41, 0xffff0000, v42
	v_lshlrev_b32_e32 v42, 16, v43
	v_and_b32_e32 v43, 0xffff0000, v43
	v_pk_fma_f32 v[34:35], v[38:39], v[138:139], v[34:35]
	v_pk_fma_f32 v[32:33], v[36:37], v[136:137], v[32:33]
	v_pk_fma_f32 v[36:37], v[30:31], v[134:135], v[42:43]
	v_pk_fma_f32 v[30:31], v[28:29], v[132:133], v[40:41]
	v_cvt_pk_bf16_f32 v28, v32, v33
	v_cvt_pk_bf16_f32 v29, v34, v35
	s_nop 0
	v_cvt_pk_bf16_f32 v30, v30, v31
	v_cvt_pk_bf16_f32 v31, v36, v37
	s_nop 0
	v_add_co_u32_e32 v36, vcc, s11, v158
	global_store_dwordx4 v[52:53], v[28:31], off
	s_nop 0
	v_addc_co_u32_e32 v37, vcc, 0, v159, vcc
	s_andn2_b64 vcc, exec, s[2:3]
	s_mov_b64 s[2:3], -1
	v_mov_b32_e32 v32, v246
	v_mov_b32_e32 v33, v247
	v_mov_b32_e32 v34, v248
	v_mov_b32_e32 v35, v249
	v_lshlrev_b32_e32 v28, 16, v32
	v_and_b32_e32 v29, 0xffff0000, v32
	v_lshlrev_b32_e32 v30, 16, v33
	v_and_b32_e32 v31, 0xffff0000, v33
	v_lshlrev_b32_e32 v32, 16, v34
	v_and_b32_e32 v33, 0xffff0000, v34
	v_lshlrev_b32_e32 v34, 16, v35
	v_and_b32_e32 v35, 0xffff0000, v35
	v_pk_fma_f32 v[26:27], v[26:27], v[122:123], v[30:31]
	v_pk_fma_f32 v[24:25], v[24:25], v[120:121], v[28:29]
	v_pk_fma_f32 v[28:29], v[18:19], v[118:119], v[34:35]
	v_pk_fma_f32 v[18:19], v[16:17], v[116:117], v[32:33]
	v_cvt_pk_bf16_f32 v16, v24, v25
	v_cvt_pk_bf16_f32 v17, v26, v27
	s_nop 0
	v_cvt_pk_bf16_f32 v18, v18, v19
	v_cvt_pk_bf16_f32 v19, v28, v29
	s_nop 0
	v_lshl_add_u64 v[28:29], v[158:159], 0, s[20:21]
	global_store_dwordx4 v[44:45], v[16:19], off offset:256
	v_mov_b32_e32 v24, v250
	v_mov_b32_e32 v25, v251
	v_mov_b32_e32 v26, v252
	v_mov_b32_e32 v27, v253
	s_nop 0
	v_lshlrev_b32_e32 v16, 16, v24
	v_and_b32_e32 v17, 0xffff0000, v24
	v_lshlrev_b32_e32 v18, 16, v25
	v_and_b32_e32 v19, 0xffff0000, v25
	v_lshlrev_b32_e32 v24, 16, v26
	v_and_b32_e32 v25, 0xffff0000, v26
	v_lshlrev_b32_e32 v26, 16, v27
	v_and_b32_e32 v27, 0xffff0000, v27
	v_pk_fma_f32 v[18:19], v[22:23], v[138:139], v[18:19]
	v_pk_fma_f32 v[16:17], v[20:21], v[136:137], v[16:17]
	v_pk_fma_f32 v[20:21], v[14:15], v[134:135], v[26:27]
	v_pk_fma_f32 v[14:15], v[12:13], v[132:133], v[24:25]
	v_cvt_pk_bf16_f32 v12, v16, v17
	v_cvt_pk_bf16_f32 v13, v18, v19
	s_nop 0
	v_cvt_pk_bf16_f32 v14, v14, v15
	v_cvt_pk_bf16_f32 v15, v20, v21
	s_nop 0
	s_nop 0
	global_store_dwordx4 v[36:37], v[12:15], off
	v_mov_b32_e32 v16, v176
	v_mov_b32_e32 v17, v177
	v_mov_b32_e32 v18, v178
	v_mov_b32_e32 v19, v179
	s_nop 0
	v_lshlrev_b32_e32 v12, 16, v16
	v_and_b32_e32 v13, 0xffff0000, v16
	v_lshlrev_b32_e32 v14, 16, v17
	v_and_b32_e32 v15, 0xffff0000, v17
	v_lshlrev_b32_e32 v16, 16, v18
	v_and_b32_e32 v17, 0xffff0000, v18
	v_lshlrev_b32_e32 v18, 16, v19
	v_and_b32_e32 v19, 0xffff0000, v19
	v_pk_fma_f32 v[8:9], v[8:9], v[120:121], v[12:13]
	v_pk_fma_f32 v[12:13], v[6:7], v[118:119], v[18:19]
	v_pk_fma_f32 v[6:7], v[4:5], v[116:117], v[16:17]
	v_pk_fma_f32 v[10:11], v[10:11], v[122:123], v[14:15]
	v_cvt_pk_bf16_f32 v4, v8, v9
	s_nop 0
	v_cvt_pk_bf16_f32 v5, v10, v11
	v_cvt_pk_bf16_f32 v6, v6, v7
	v_cvt_pk_bf16_f32 v7, v12, v13
	global_store_dwordx4 v[28:29], v[4:7], off offset:256
	s_cbranch_vccnz .LBB0_3160
	s_andn2_b64 vcc, exec, s[4:5]
	s_cbranch_vccnz .LBB0_3159
	s_barrier
	s_branch .LBB0_3159
